# v3
# baseline (speedup 1.0000x reference)
.LBB0_78:
	s_or_b64 exec, exec, s[4:5]
	s_waitcnt lgkmcnt(0)
	s_barrier
	s_and_saveexec_b64 s[4:5], s[10:11]
	s_cbranch_execz .LBB0_81
	v_mov_b32_e32 v1, 0x23440
	v_mov_b32_e32 v6, 0x23450
	ds_read_b128 v[2:5], v1
	ds_read_b128 v[6:9], v6
	v_mov_b32_e32 v1, 0x23460
	ds_read_b128 v[10:13], v1
	s_mov_b32 s3, 0x3fb8aa3b
	s_waitcnt lgkmcnt(2)
	v_add_f32_e32 v1, s6, v2
	v_mov_b32_e32 v2, 0x23470
	ds_read_b128 v[14:17], v2
	v_mov_b32_e32 v2, 0x23480
	s_waitcnt lgkmcnt(2)
	v_add_f32_e32 v1, v1, v6
	v_mov_b32_e32 v6, 0x23490
	ds_read_b128 v[18:21], v2
	ds_read_b128 v[22:25], v6
	v_mov_b32_e32 v2, 0x234a0
	v_mov_b32_e32 v6, 0x234b0
	ds_read_b128 v[26:29], v2
	ds_read_b128 v[30:33], v6
	v_add_f32_e32 v2, s6, v3
	v_add_f32_e32 v2, v2, v7
	s_waitcnt lgkmcnt(5)
	v_add_f32_e32 v2, v2, v11
	s_waitcnt lgkmcnt(4)
	v_add_f32_e32 v2, v2, v15
	s_waitcnt lgkmcnt(3)
	v_add_f32_e32 v2, v2, v19
	s_waitcnt lgkmcnt(2)
	v_add_f32_e32 v2, v2, v23
	s_waitcnt lgkmcnt(1)
	v_add_f32_e32 v2, v2, v27
	s_waitcnt lgkmcnt(0)
	v_add_f32_e32 v3, v2, v31
	v_add_f32_e32 v2, s6, v4
	v_add_f32_e32 v2, v2, v8
	v_add_f32_e32 v2, v2, v12
	v_add_f32_e32 v2, v2, v16
	v_add_f32_e32 v2, v2, v20
	v_add_f32_e32 v2, v2, v24
	v_add_f32_e32 v2, v2, v28
	v_add_f32_e32 v6, v2, v32
	v_add_f32_e32 v2, s6, v5
	v_add_f32_e32 v2, v2, v9
	v_add_f32_e32 v2, v2, v13
	v_add_f32_e32 v1, v1, v10
	v_add_f32_e32 v2, v2, v17
	v_add_f32_e32 v1, v1, v14
	v_add_f32_e32 v2, v2, v21
	v_add_f32_e32 v1, v1, v18
	v_add_f32_e32 v2, v2, v25
	v_add_f32_e32 v1, v1, v22
	v_add_f32_e32 v2, v2, v29
	v_add_f32_e32 v1, v1, v26
	v_add_f32_e32 v10, v2, v33
	v_add_f32_e32 v1, v1, v30
	v_max_f32_e32 v2, v6, v10
	v_max3_f32 v2, v1, v3, v2
	v_sub_f32_e32 v1, v1, v2
	v_mul_f32_e32 v4, 0x3fb8aa3b, v1
	v_fma_f32 v5, v1, s3, -v4
	v_rndne_f32_e32 v7, v4
	v_fmac_f32_e32 v5, 0x32a5705f, v1
	v_sub_f32_e32 v4, v4, v7
	v_add_f32_e32 v4, v4, v5
	v_exp_f32_e32 v4, v4
	v_cvt_i32_f32_e32 v5, v7
	v_sub_f32_e32 v3, v3, v2
	v_mul_f32_e32 v12, 0x3fb8aa3b, v3
	s_mov_b32 s4, 0xc2ce8ed0
	v_fma_f32 v13, v3, s3, -v12
	v_rndne_f32_e32 v14, v12
	v_add_u32_e32 v8, 0x22c00, v130
	v_ldexp_f32 v4, v4, v5
	v_cmp_ngt_f32_e32 vcc, s4, v1
	v_fmac_f32_e32 v13, 0x32a5705f, v3
	v_sub_f32_e32 v12, v12, v14
	v_cndmask_b32_e32 v9, 0, v4, vcc
	ds_read2st64_b32 v[4:5], v8 offset1:2
	v_add_f32_e32 v12, v12, v13
	v_exp_f32_e32 v12, v12
	v_cvt_i32_f32_e32 v13, v14
	s_mov_b32 s5, 0x42b17218
	v_mov_b32_e32 v11, 0x7f800000
	v_cmp_nlt_f32_e32 vcc, s5, v1
	v_sub_f32_e32 v6, v6, v2
	v_mov_b32_e32 v7, 0
	v_cndmask_b32_e32 v1, v11, v9, vcc
	v_mul_f32_e32 v9, 0x3fb8aa3b, v6
	s_waitcnt lgkmcnt(0)
	v_fma_f32 v14, v1, v4, 0
	v_ldexp_f32 v4, v12, v13
	v_fma_f32 v12, v6, s3, -v9
	v_rndne_f32_e32 v13, v9
	v_fmac_f32_e32 v12, 0x32a5705f, v6
	v_sub_f32_e32 v9, v9, v13
	v_cmp_ngt_f32_e32 vcc, s4, v3
	v_add_f32_e32 v9, v9, v12
	v_exp_f32_e32 v9, v9
	v_cndmask_b32_e32 v4, 0, v4, vcc
	v_cvt_i32_f32_e32 v12, v13
	v_cmp_nlt_f32_e32 vcc, s5, v3
	s_nop 1
	v_cndmask_b32_e32 v3, v11, v4, vcc
	v_fmac_f32_e32 v14, v3, v5
	v_sub_f32_e32 v5, v10, v2
	v_mul_f32_e32 v10, 0x3fb8aa3b, v5
	v_ldexp_f32 v4, v9, v12
	v_fma_f32 v12, v5, s3, -v10
	v_rndne_f32_e32 v13, v10
	v_fmac_f32_e32 v12, 0x32a5705f, v5
	v_sub_f32_e32 v10, v10, v13
	v_add_f32_e32 v10, v10, v12
	v_exp_f32_e32 v10, v10
	v_cvt_i32_f32_e32 v12, v13
	ds_read2st64_b32 v[8:9], v8 offset0:4 offset1:6
	v_cmp_ngt_f32_e32 vcc, s4, v6
	s_nop 1
	v_cndmask_b32_e32 v4, 0, v4, vcc
	v_cmp_nlt_f32_e32 vcc, s5, v6
	v_ldexp_f32 v6, v10, v12
	s_nop 0
	v_cndmask_b32_e32 v4, v11, v4, vcc
	v_cmp_ngt_f32_e32 vcc, s4, v5
	s_waitcnt lgkmcnt(0)
	v_fmac_f32_e32 v14, v4, v8
	v_cndmask_b32_e32 v6, 0, v6, vcc
	v_cmp_nlt_f32_e32 vcc, s5, v5
	s_nop 1
	v_cndmask_b32_e32 v5, v11, v6, vcc
	s_lshl_b32 s36, s2, 7
	v_add_u32_e32 v6, s36, v0
	v_fmac_f32_e32 v14, v5, v9
	v_lshl_add_u64 v[6:7], v[6:7], 2, s[20:21]
	global_store_dword v[6:7], v14, off
	s_and_b64 exec, exec, s[0:1]
	s_cbranch_execz .LBB0_81
	s_lshl_b32 s0, s2, 1
	s_mov_b32 s1, 0
	v_add_f32_e32 v0, v1, v3
	s_lshl_b64 s[0:1], s[0:1], 2
	v_add_f32_e32 v0, v0, v4
	s_add_u32 s0, s20, s0
	v_add_f32_e32 v3, v0, v5
	s_addc_u32 s1, s21, s1
	v_mov_b32_e32 v0, 0x20000
	global_store_dwordx2 v0, v[2:3], s[0:1]

_Z12pool3_kernelPKfS0_Pf:
	s_load_dwordx4 s[4:7], s[0:1], 0x0
	s_load_dwordx2 s[8:9], s[0:1], 0x10
	v_and_b32_e32 v1, 63, v0
	v_lshrrev_b32_e32 v2, 6, v0
	v_lshlrev_b32_e32 v3, 3, v1
	v_lshlrev_b32_e32 v4, 3, v0
	v_lshl_add_u32 v5, v2, 15, v3
	s_lshl_b32 s12, s2, 13
	s_lshl_b32 s13, s2, 6
	v_lshl_add_u32 v6, v0, 5, s12
	v_lshrrev_b32_e32 v7, 4, v0
	v_lshl_add_u32 v7, v7, 2, s13
	s_waitcnt lgkmcnt(0)
	s_add_u32 s10, s4, 0x20000
	s_addc_u32 s11, s5, 0
	global_load_dwordx2 v[10:11], v3, s[10:11]
	global_load_dwordx2 v[12:13], v3, s[10:11] offset:512
	global_load_dwordx2 v[14:15], v3, s[10:11] offset:1024
	global_load_dwordx2 v[16:17], v3, s[10:11] offset:1536
	global_load_dwordx2 v[18:19], v4, s[10:11]
	global_load_dwordx4 v[20:23], v6, s[6:7]
	global_load_dwordx4 v[24:27], v6, s[6:7] offset:16
	global_load_dword v28, v7, s[8:9]
	v_add_u32_e32 v31, 0x1000, v5
	v_add_u32_e32 v32, 0x2000, v5
	v_add_u32_e32 v33, 0x3000, v5
	v_add_u32_e32 v34, 0x4000, v5
	v_add_u32_e32 v35, 0x5000, v5
	v_add_u32_e32 v36, 0x6000, v5
	v_add_u32_e32 v37, 0x7000, v5
	global_load_dwordx2 v[64:65], v5, s[4:5]
	global_load_dwordx2 v[66:67], v5, s[4:5] offset:512
	global_load_dwordx2 v[68:69], v5, s[4:5] offset:1024
	global_load_dwordx2 v[70:71], v5, s[4:5] offset:1536
	global_load_dwordx2 v[72:73], v5, s[4:5] offset:2048
	global_load_dwordx2 v[74:75], v5, s[4:5] offset:2560
	global_load_dwordx2 v[76:77], v5, s[4:5] offset:3072
	global_load_dwordx2 v[78:79], v5, s[4:5] offset:3584
	global_load_dwordx2 v[80:81], v31, s[4:5]
	global_load_dwordx2 v[82:83], v31, s[4:5] offset:512
	global_load_dwordx2 v[84:85], v31, s[4:5] offset:1024
	global_load_dwordx2 v[86:87], v31, s[4:5] offset:1536
	global_load_dwordx2 v[88:89], v31, s[4:5] offset:2048
	global_load_dwordx2 v[90:91], v31, s[4:5] offset:2560
	global_load_dwordx2 v[92:93], v31, s[4:5] offset:3072
	global_load_dwordx2 v[94:95], v31, s[4:5] offset:3584
	global_load_dwordx2 v[96:97], v32, s[4:5]
	global_load_dwordx2 v[98:99], v32, s[4:5] offset:512
	global_load_dwordx2 v[100:101], v32, s[4:5] offset:1024
	global_load_dwordx2 v[102:103], v32, s[4:5] offset:1536
	global_load_dwordx2 v[104:105], v32, s[4:5] offset:2048
	global_load_dwordx2 v[106:107], v32, s[4:5] offset:2560
	global_load_dwordx2 v[108:109], v32, s[4:5] offset:3072
	global_load_dwordx2 v[110:111], v32, s[4:5] offset:3584
	global_load_dwordx2 v[112:113], v33, s[4:5]
	global_load_dwordx2 v[114:115], v33, s[4:5] offset:512
	global_load_dwordx2 v[116:117], v33, s[4:5] offset:1024
	global_load_dwordx2 v[118:119], v33, s[4:5] offset:1536
	global_load_dwordx2 v[120:121], v33, s[4:5] offset:2048
	global_load_dwordx2 v[122:123], v33, s[4:5] offset:2560
	global_load_dwordx2 v[124:125], v33, s[4:5] offset:3072
	global_load_dwordx2 v[126:127], v33, s[4:5] offset:3584
	global_load_dwordx2 v[128:129], v34, s[4:5]
	global_load_dwordx2 v[130:131], v34, s[4:5] offset:512
	global_load_dwordx2 v[132:133], v34, s[4:5] offset:1024
	global_load_dwordx2 v[134:135], v34, s[4:5] offset:1536
	global_load_dwordx2 v[136:137], v34, s[4:5] offset:2048
	global_load_dwordx2 v[138:139], v34, s[4:5] offset:2560
	global_load_dwordx2 v[140:141], v34, s[4:5] offset:3072
	global_load_dwordx2 v[142:143], v34, s[4:5] offset:3584
	global_load_dwordx2 v[144:145], v35, s[4:5]
	global_load_dwordx2 v[146:147], v35, s[4:5] offset:512
	global_load_dwordx2 v[148:149], v35, s[4:5] offset:1024
	global_load_dwordx2 v[150:151], v35, s[4:5] offset:1536
	global_load_dwordx2 v[152:153], v35, s[4:5] offset:2048
	global_load_dwordx2 v[154:155], v35, s[4:5] offset:2560
	global_load_dwordx2 v[156:157], v35, s[4:5] offset:3072
	global_load_dwordx2 v[158:159], v35, s[4:5] offset:3584
	global_load_dwordx2 v[160:161], v36, s[4:5]
	global_load_dwordx2 v[162:163], v36, s[4:5] offset:512
	global_load_dwordx2 v[164:165], v36, s[4:5] offset:1024
	global_load_dwordx2 v[166:167], v36, s[4:5] offset:1536
	global_load_dwordx2 v[168:169], v36, s[4:5] offset:2048
	global_load_dwordx2 v[170:171], v36, s[4:5] offset:2560
	global_load_dwordx2 v[172:173], v36, s[4:5] offset:3072
	s_waitcnt vmcnt(55)
	v_max_f32_e32 v40, v10, v12
	v_max_f32_e32 v41, v14, v16
	v_max_f32_e32 v40, v40, v41
	s_nop 1
	v_max_f32_dpp v40, v40, v40 row_shr:1 row_mask:0xf bank_mask:0xf
	s_nop 1
	v_max_f32_dpp v40, v40, v40 row_shr:2 row_mask:0xf bank_mask:0xf
	s_nop 1
	v_max_f32_dpp v40, v40, v40 row_shr:4 row_mask:0xf bank_mask:0xf
	s_nop 1
	v_max_f32_dpp v40, v40, v40 row_shr:8 row_mask:0xf bank_mask:0xf
	s_nop 1
	v_readlane_b32 s16, v40, 15
	v_readlane_b32 s17, v40, 31
	v_readlane_b32 s18, v40, 47
	v_readlane_b32 s19, v40, 63
	s_nop 1
	v_mov_b32_e32 v41, s16
	v_max_f32_e32 v41, s17, v41
	v_max_f32_e32 v41, s18, v41
	v_max_f32_e32 v41, s19, v41
	v_sub_f32_e32 v42, v10, v41
	v_sub_f32_e32 v43, v12, v41
	v_sub_f32_e32 v44, v14, v41
	v_sub_f32_e32 v45, v16, v41
	v_sub_f32_e32 v46, v18, v41
	v_mul_f32_e32 v42, 0x3fb8aa3b, v42
	v_mul_f32_e32 v43, 0x3fb8aa3b, v43
	v_mul_f32_e32 v44, 0x3fb8aa3b, v44
	v_mul_f32_e32 v45, 0x3fb8aa3b, v45
	v_mul_f32_e32 v46, 0x3fb8aa3b, v46
	v_exp_f32_e32 v42, v42
	v_exp_f32_e32 v43, v43
	v_exp_f32_e32 v44, v44
	v_exp_f32_e32 v45, v45
	v_exp_f32_e32 v46, v46
	s_nop 0
	v_mul_f32_e32 v47, v11, v42
	v_fmac_f32_e32 v47, v13, v43
	v_fmac_f32_e32 v47, v15, v44
	v_fmac_f32_e32 v47, v17, v45
	s_nop 1
	v_add_f32_dpp v47, v47, v47 row_shr:1 row_mask:0xf bank_mask:0xf
	s_nop 1
	v_add_f32_dpp v47, v47, v47 row_shr:2 row_mask:0xf bank_mask:0xf
	s_nop 1
	v_add_f32_dpp v47, v47, v47 row_shr:4 row_mask:0xf bank_mask:0xf
	s_nop 1
	v_add_f32_dpp v47, v47, v47 row_shr:8 row_mask:0xf bank_mask:0xf
	s_nop 1
	v_readlane_b32 s20, v47, 15
	v_readlane_b32 s21, v47, 31
	v_readlane_b32 s22, v47, 47
	v_readlane_b32 s23, v47, 63
	s_nop 1
	v_mov_b32_e32 v48, s20
	v_add_f32_e32 v48, s21, v48
	v_add_f32_e32 v48, s22, v48
	v_add_f32_e32 v48, s23, v48
	v_rcp_f32_e32 v49, v48
	v_mov_b32_e32 v50, 0
	v_mov_b32_e32 v51, 0
	v_mov_b32_e32 v52, 0
	v_mov_b32_e32 v53, 0
	v_readlane_b32 s24, v46, 0
	v_readlane_b32 s26, v46, 1
	v_readlane_b32 s28, v46, 2
	v_readlane_b32 s30, v46, 3
	s_waitcnt vmcnt(54)
	v_pk_fma_f32 v[50:51], v[64:65], s[24:25], v[50:51] op_sel_hi:[1,0,1]
	global_load_dwordx2 v[174:175], v36, s[4:5] offset:3584
	v_readlane_b32 s24, v46, 4
	s_waitcnt vmcnt(54)
	v_pk_fma_f32 v[52:53], v[66:67], s[26:27], v[52:53] op_sel_hi:[1,0,1]
	global_load_dwordx2 v[176:177], v37, s[4:5]
	v_readlane_b32 s26, v46, 5
	s_waitcnt vmcnt(54)
	v_pk_fma_f32 v[50:51], v[68:69], s[28:29], v[50:51] op_sel_hi:[1,0,1]
	global_load_dwordx2 v[178:179], v37, s[4:5] offset:512
	v_readlane_b32 s28, v46, 6
	s_waitcnt vmcnt(54)
	v_pk_fma_f32 v[52:53], v[70:71], s[30:31], v[52:53] op_sel_hi:[1,0,1]
	global_load_dwordx2 v[180:181], v37, s[4:5] offset:1024
	v_readlane_b32 s30, v46, 7
	s_waitcnt vmcnt(54)
	v_pk_fma_f32 v[50:51], v[72:73], s[24:25], v[50:51] op_sel_hi:[1,0,1]
	global_load_dwordx2 v[182:183], v37, s[4:5] offset:1536
	v_readlane_b32 s24, v46, 8
	s_waitcnt vmcnt(54)
	v_pk_fma_f32 v[52:53], v[74:75], s[26:27], v[52:53] op_sel_hi:[1,0,1]
	global_load_dwordx2 v[184:185], v37, s[4:5] offset:2048
	v_readlane_b32 s26, v46, 9
	s_waitcnt vmcnt(54)
	v_pk_fma_f32 v[50:51], v[76:77], s[28:29], v[50:51] op_sel_hi:[1,0,1]
	global_load_dwordx2 v[186:187], v37, s[4:5] offset:2560
	v_readlane_b32 s28, v46, 10
	s_waitcnt vmcnt(54)
	v_pk_fma_f32 v[52:53], v[78:79], s[30:31], v[52:53] op_sel_hi:[1,0,1]
	global_load_dwordx2 v[188:189], v37, s[4:5] offset:3072
	v_readlane_b32 s30, v46, 11
	s_waitcnt vmcnt(54)
	v_pk_fma_f32 v[50:51], v[80:81], s[24:25], v[50:51] op_sel_hi:[1,0,1]
	global_load_dwordx2 v[190:191], v37, s[4:5] offset:3584
	v_readlane_b32 s24, v46, 12
	s_waitcnt vmcnt(54)
	v_pk_fma_f32 v[52:53], v[82:83], s[26:27], v[52:53] op_sel_hi:[1,0,1]
	v_readlane_b32 s26, v46, 13
	s_waitcnt vmcnt(53)
	v_pk_fma_f32 v[50:51], v[84:85], s[28:29], v[50:51] op_sel_hi:[1,0,1]
	v_readlane_b32 s28, v46, 14
	s_waitcnt vmcnt(52)
	v_pk_fma_f32 v[52:53], v[86:87], s[30:31], v[52:53] op_sel_hi:[1,0,1]
	v_readlane_b32 s30, v46, 15
	s_waitcnt vmcnt(51)
	v_pk_fma_f32 v[50:51], v[88:89], s[24:25], v[50:51] op_sel_hi:[1,0,1]
	v_readlane_b32 s24, v46, 16
	s_waitcnt vmcnt(50)
	v_pk_fma_f32 v[52:53], v[90:91], s[26:27], v[52:53] op_sel_hi:[1,0,1]
	v_readlane_b32 s26, v46, 17
	s_waitcnt vmcnt(49)
	v_pk_fma_f32 v[50:51], v[92:93], s[28:29], v[50:51] op_sel_hi:[1,0,1]
	v_readlane_b32 s28, v46, 18
	s_waitcnt vmcnt(48)
	v_pk_fma_f32 v[52:53], v[94:95], s[30:31], v[52:53] op_sel_hi:[1,0,1]
	v_readlane_b32 s30, v46, 19
	s_waitcnt vmcnt(47)
	v_pk_fma_f32 v[50:51], v[96:97], s[24:25], v[50:51] op_sel_hi:[1,0,1]
	v_readlane_b32 s24, v46, 20
	s_waitcnt vmcnt(46)
	v_pk_fma_f32 v[52:53], v[98:99], s[26:27], v[52:53] op_sel_hi:[1,0,1]
	v_readlane_b32 s26, v46, 21
	s_waitcnt vmcnt(45)
	v_pk_fma_f32 v[50:51], v[100:101], s[28:29], v[50:51] op_sel_hi:[1,0,1]
	v_readlane_b32 s28, v46, 22
	s_waitcnt vmcnt(44)
	v_pk_fma_f32 v[52:53], v[102:103], s[30:31], v[52:53] op_sel_hi:[1,0,1]
	v_readlane_b32 s30, v46, 23
	s_waitcnt vmcnt(43)
	v_pk_fma_f32 v[50:51], v[104:105], s[24:25], v[50:51] op_sel_hi:[1,0,1]
	v_readlane_b32 s24, v46, 24
	s_waitcnt vmcnt(42)
	v_pk_fma_f32 v[52:53], v[106:107], s[26:27], v[52:53] op_sel_hi:[1,0,1]
	v_readlane_b32 s26, v46, 25
	s_waitcnt vmcnt(41)
	v_pk_fma_f32 v[50:51], v[108:109], s[28:29], v[50:51] op_sel_hi:[1,0,1]
	v_readlane_b32 s28, v46, 26
	s_waitcnt vmcnt(40)
	v_pk_fma_f32 v[52:53], v[110:111], s[30:31], v[52:53] op_sel_hi:[1,0,1]
	v_readlane_b32 s30, v46, 27
	s_waitcnt vmcnt(39)
	v_pk_fma_f32 v[50:51], v[112:113], s[24:25], v[50:51] op_sel_hi:[1,0,1]
	v_readlane_b32 s24, v46, 28
	s_waitcnt vmcnt(38)
	v_pk_fma_f32 v[52:53], v[114:115], s[26:27], v[52:53] op_sel_hi:[1,0,1]
	v_readlane_b32 s26, v46, 29
	s_waitcnt vmcnt(37)
	v_pk_fma_f32 v[50:51], v[116:117], s[28:29], v[50:51] op_sel_hi:[1,0,1]
	v_readlane_b32 s28, v46, 30
	s_waitcnt vmcnt(36)
	v_pk_fma_f32 v[52:53], v[118:119], s[30:31], v[52:53] op_sel_hi:[1,0,1]
	v_readlane_b32 s30, v46, 31
	s_waitcnt vmcnt(35)
	v_pk_fma_f32 v[50:51], v[120:121], s[24:25], v[50:51] op_sel_hi:[1,0,1]
	v_readlane_b32 s24, v46, 32
	s_waitcnt vmcnt(34)
	v_pk_fma_f32 v[52:53], v[122:123], s[26:27], v[52:53] op_sel_hi:[1,0,1]
	v_readlane_b32 s26, v46, 33
	s_waitcnt vmcnt(33)
	v_pk_fma_f32 v[50:51], v[124:125], s[28:29], v[50:51] op_sel_hi:[1,0,1]
	v_readlane_b32 s28, v46, 34
	s_waitcnt vmcnt(32)
	v_pk_fma_f32 v[52:53], v[126:127], s[30:31], v[52:53] op_sel_hi:[1,0,1]
	v_readlane_b32 s30, v46, 35
	s_waitcnt vmcnt(31)
	v_pk_fma_f32 v[50:51], v[128:129], s[24:25], v[50:51] op_sel_hi:[1,0,1]
	v_readlane_b32 s24, v46, 36
	s_waitcnt vmcnt(30)
	v_pk_fma_f32 v[52:53], v[130:131], s[26:27], v[52:53] op_sel_hi:[1,0,1]
	v_readlane_b32 s26, v46, 37
	s_waitcnt vmcnt(29)
	v_pk_fma_f32 v[50:51], v[132:133], s[28:29], v[50:51] op_sel_hi:[1,0,1]
	v_readlane_b32 s28, v46, 38
	s_waitcnt vmcnt(28)
	v_pk_fma_f32 v[52:53], v[134:135], s[30:31], v[52:53] op_sel_hi:[1,0,1]
	v_readlane_b32 s30, v46, 39
	s_waitcnt vmcnt(27)
	v_pk_fma_f32 v[50:51], v[136:137], s[24:25], v[50:51] op_sel_hi:[1,0,1]
	v_readlane_b32 s24, v46, 40
	s_waitcnt vmcnt(26)
	v_pk_fma_f32 v[52:53], v[138:139], s[26:27], v[52:53] op_sel_hi:[1,0,1]
	v_readlane_b32 s26, v46, 41
	s_waitcnt vmcnt(25)
	v_pk_fma_f32 v[50:51], v[140:141], s[28:29], v[50:51] op_sel_hi:[1,0,1]
	v_readlane_b32 s28, v46, 42
	s_waitcnt vmcnt(24)
	v_pk_fma_f32 v[52:53], v[142:143], s[30:31], v[52:53] op_sel_hi:[1,0,1]
	v_readlane_b32 s30, v46, 43
	s_waitcnt vmcnt(23)
	v_pk_fma_f32 v[50:51], v[144:145], s[24:25], v[50:51] op_sel_hi:[1,0,1]
	v_readlane_b32 s24, v46, 44
	s_waitcnt vmcnt(22)
	v_pk_fma_f32 v[52:53], v[146:147], s[26:27], v[52:53] op_sel_hi:[1,0,1]
	v_readlane_b32 s26, v46, 45
	s_waitcnt vmcnt(21)
	v_pk_fma_f32 v[50:51], v[148:149], s[28:29], v[50:51] op_sel_hi:[1,0,1]
	v_readlane_b32 s28, v46, 46
	s_waitcnt vmcnt(20)
	v_pk_fma_f32 v[52:53], v[150:151], s[30:31], v[52:53] op_sel_hi:[1,0,1]
	v_readlane_b32 s30, v46, 47
	s_waitcnt vmcnt(19)
	v_pk_fma_f32 v[50:51], v[152:153], s[24:25], v[50:51] op_sel_hi:[1,0,1]
	v_readlane_b32 s24, v46, 48
	s_waitcnt vmcnt(18)
	v_pk_fma_f32 v[52:53], v[154:155], s[26:27], v[52:53] op_sel_hi:[1,0,1]
	v_readlane_b32 s26, v46, 49
	s_waitcnt vmcnt(17)
	v_pk_fma_f32 v[50:51], v[156:157], s[28:29], v[50:51] op_sel_hi:[1,0,1]
	v_readlane_b32 s28, v46, 50
	s_waitcnt vmcnt(16)
	v_pk_fma_f32 v[52:53], v[158:159], s[30:31], v[52:53] op_sel_hi:[1,0,1]
	v_readlane_b32 s30, v46, 51
	s_waitcnt vmcnt(15)
	v_pk_fma_f32 v[50:51], v[160:161], s[24:25], v[50:51] op_sel_hi:[1,0,1]
	v_readlane_b32 s24, v46, 52
	s_waitcnt vmcnt(14)
	v_pk_fma_f32 v[52:53], v[162:163], s[26:27], v[52:53] op_sel_hi:[1,0,1]
	v_readlane_b32 s26, v46, 53
	s_waitcnt vmcnt(13)
	v_pk_fma_f32 v[50:51], v[164:165], s[28:29], v[50:51] op_sel_hi:[1,0,1]
	v_readlane_b32 s28, v46, 54
	s_waitcnt vmcnt(12)
	v_pk_fma_f32 v[52:53], v[166:167], s[30:31], v[52:53] op_sel_hi:[1,0,1]
	v_readlane_b32 s30, v46, 55
	s_waitcnt vmcnt(11)
	v_pk_fma_f32 v[50:51], v[168:169], s[24:25], v[50:51] op_sel_hi:[1,0,1]
	v_readlane_b32 s24, v46, 56
	s_waitcnt vmcnt(10)
	v_pk_fma_f32 v[52:53], v[170:171], s[26:27], v[52:53] op_sel_hi:[1,0,1]
	v_readlane_b32 s26, v46, 57
	s_waitcnt vmcnt(9)
	v_pk_fma_f32 v[50:51], v[172:173], s[28:29], v[50:51] op_sel_hi:[1,0,1]
	v_readlane_b32 s28, v46, 58
	s_waitcnt vmcnt(8)
	v_pk_fma_f32 v[52:53], v[174:175], s[30:31], v[52:53] op_sel_hi:[1,0,1]
	v_readlane_b32 s30, v46, 59
	s_waitcnt vmcnt(7)
	v_pk_fma_f32 v[50:51], v[176:177], s[24:25], v[50:51] op_sel_hi:[1,0,1]
	v_readlane_b32 s24, v46, 60
	s_waitcnt vmcnt(6)
	v_pk_fma_f32 v[52:53], v[178:179], s[26:27], v[52:53] op_sel_hi:[1,0,1]
	v_readlane_b32 s26, v46, 61
	s_waitcnt vmcnt(5)
	v_pk_fma_f32 v[50:51], v[180:181], s[28:29], v[50:51] op_sel_hi:[1,0,1]
	v_readlane_b32 s28, v46, 62
	s_waitcnt vmcnt(4)
	v_pk_fma_f32 v[52:53], v[182:183], s[30:31], v[52:53] op_sel_hi:[1,0,1]
	v_readlane_b32 s30, v46, 63
	s_waitcnt vmcnt(3)
	v_pk_fma_f32 v[50:51], v[184:185], s[24:25], v[50:51] op_sel_hi:[1,0,1]
	s_waitcnt vmcnt(2)
	v_pk_fma_f32 v[52:53], v[186:187], s[26:27], v[52:53] op_sel_hi:[1,0,1]
	s_waitcnt vmcnt(1)
	v_pk_fma_f32 v[50:51], v[188:189], s[28:29], v[50:51] op_sel_hi:[1,0,1]
	s_waitcnt vmcnt(0)
	v_pk_fma_f32 v[52:53], v[190:191], s[30:31], v[52:53] op_sel_hi:[1,0,1]
	v_pk_add_f32 v[50:51], v[50:51], v[52:53]
	v_lshl_add_u32 v54, v2, 9, v3
	ds_write_b64 v54, v[50:51]
	v_and_b32_e32 v55, 15, v0
	v_lshlrev_b32_e32 v56, 5, v55
	s_waitcnt lgkmcnt(0)
	s_barrier
	ds_read_b128 v[64:67], v56 offset:0
	ds_read_b128 v[68:71], v56 offset:16
	ds_read_b128 v[72:75], v56 offset:512
	ds_read_b128 v[76:79], v56 offset:528
	ds_read_b128 v[80:83], v56 offset:1024
	ds_read_b128 v[84:87], v56 offset:1040
	ds_read_b128 v[88:91], v56 offset:1536
	ds_read_b128 v[92:95], v56 offset:1552
	s_waitcnt lgkmcnt(4)
	v_pk_add_f32 v[64:65], v[64:65], v[72:73]
	v_pk_add_f32 v[66:67], v[66:67], v[74:75]
	v_pk_add_f32 v[68:69], v[68:69], v[76:77]
	v_pk_add_f32 v[70:71], v[70:71], v[78:79]
	s_waitcnt lgkmcnt(2)
	v_pk_add_f32 v[64:65], v[64:65], v[80:81]
	v_pk_add_f32 v[66:67], v[66:67], v[82:83]
	v_pk_add_f32 v[68:69], v[68:69], v[84:85]
	v_pk_add_f32 v[70:71], v[70:71], v[86:87]
	s_waitcnt lgkmcnt(0)
	v_pk_add_f32 v[64:65], v[64:65], v[88:89]
	v_pk_add_f32 v[66:67], v[66:67], v[90:91]
	v_pk_add_f32 v[68:69], v[68:69], v[92:93]
	v_pk_add_f32 v[70:71], v[70:71], v[94:95]
	v_mul_f32_e32 v57, v64, v20
	v_fmac_f32_e32 v57, v65, v21
	v_fmac_f32_e32 v57, v66, v22
	v_fmac_f32_e32 v57, v67, v23
	v_fmac_f32_e32 v57, v68, v24
	v_fmac_f32_e32 v57, v69, v25
	v_fmac_f32_e32 v57, v70, v26
	v_fmac_f32_e32 v57, v71, v27
	s_nop 1
	v_add_f32_dpp v57, v57, v57 row_shr:1 row_mask:0xf bank_mask:0xf
	s_nop 1
	v_add_f32_dpp v57, v57, v57 row_shr:2 row_mask:0xf bank_mask:0xf
	s_nop 1
	v_add_f32_dpp v57, v57, v57 row_shr:4 row_mask:0xf bank_mask:0xf
	s_nop 1
	v_add_f32_dpp v57, v57, v57 row_shr:8 row_mask:0xf bank_mask:0xf
	v_cmp_eq_u32_e32 vcc, 15, v55
	v_fma_f32 v58, v57, v49, v28
	s_and_saveexec_b64 s[14:15], vcc
	global_store_dword v7, v58, s[8:9]
	s_endpgm

	.amdhsa_kernel _Z12pool3_kernelPKfS0_Pf
		.amdhsa_group_segment_fixed_size 18592
		.amdhsa_private_segment_fixed_size 0
		.amdhsa_kernarg_size 24
		.amdhsa_user_sgpr_count 2
		.amdhsa_user_sgpr_dispatch_ptr 0
		.amdhsa_user_sgpr_queue_ptr 0
		.amdhsa_user_sgpr_kernarg_segment_ptr 1
		.amdhsa_user_sgpr_dispatch_id 0
		.amdhsa_user_sgpr_kernarg_preload_length 0
		.amdhsa_user_sgpr_kernarg_preload_offset 0
		.amdhsa_user_sgpr_private_segment_size 0
		.amdhsa_uses_dynamic_stack 0
		.amdhsa_enable_private_segment 0
		.amdhsa_system_sgpr_workgroup_id_x 1
		.amdhsa_system_sgpr_workgroup_id_y 0
		.amdhsa_system_sgpr_workgroup_id_z 0
		.amdhsa_system_sgpr_workgroup_info 0
		.amdhsa_system_vgpr_workitem_id 0
		.amdhsa_next_free_vgpr 192
		.amdhsa_next_free_sgpr 32
		.amdhsa_accum_offset 192
		.amdhsa_reserve_vcc 1
		.amdhsa_float_round_mode_32 0
		.amdhsa_float_round_mode_16_64 0
		.amdhsa_float_denorm_mode_32 3
		.amdhsa_float_denorm_mode_16_64 3
		.amdhsa_dx10_clamp 1
		.amdhsa_ieee_mode 1
		.amdhsa_fp16_overflow 0
		.amdhsa_tg_split 0
		.amdhsa_exception_fp_ieee_invalid_op 0
		.amdhsa_exception_fp_denorm_src 0
		.amdhsa_exception_fp_ieee_div_zero 0
		.amdhsa_exception_fp_ieee_overflow 0
		.amdhsa_exception_fp_ieee_underflow 0
		.amdhsa_exception_fp_ieee_inexact 0
		.amdhsa_exception_int_div_zero 0
	.end_amdhsa_kernel

.Lfunc_end1:
	.size	_Z12pool3_kernelPKfS0_Pf, .Lfunc_end1-_Z12pool3_kernelPKfS0_Pf
	.set _Z12pool3_kernelPKfS0_Pf.num_vgpr, 192
	.set _Z12pool3_kernelPKfS0_Pf.num_agpr, 0
	.set _Z12pool3_kernelPKfS0_Pf.numbered_sgpr, 32
	.set _Z12pool3_kernelPKfS0_Pf.num_named_barrier, 0
	.set _Z12pool3_kernelPKfS0_Pf.private_seg_size, 0
	.set _Z12pool3_kernelPKfS0_Pf.uses_vcc, 1
	.set _Z12pool3_kernelPKfS0_Pf.uses_flat_scratch, 0
	.set _Z12pool3_kernelPKfS0_Pf.has_dyn_sized_stack, 0
	.set _Z12pool3_kernelPKfS0_Pf.has_recursion, 0
	.set _Z12pool3_kernelPKfS0_Pf.has_indirect_call, 0

amdhsa.kernels:
  - .agpr_count:     0
    .args:
      - .actual_access:  read_only
        .address_space:  global
        .offset:         0
        .size:           8
        .value_kind:     global_buffer
      - .actual_access:  read_only
        .address_space:  global
        .offset:         8
        .size:           8
        .value_kind:     global_buffer
      - .actual_access:  read_only
        .address_space:  global
        .offset:         16
        .size:           8
        .value_kind:     global_buffer
      - .actual_access:  read_only
        .address_space:  global
        .offset:         24
        .size:           8
        .value_kind:     global_buffer
      - .actual_access:  read_only
        .address_space:  global
        .offset:         32
        .size:           8
        .value_kind:     global_buffer
      - .actual_access:  read_only
        .address_space:  global
        .offset:         40
        .size:           8
        .value_kind:     global_buffer
      - .actual_access:  read_only
        .address_space:  global
        .offset:         48
        .size:           8
        .value_kind:     global_buffer
      - .actual_access:  read_only
        .address_space:  global
        .offset:         56
        .size:           8
        .value_kind:     global_buffer
      - .actual_access:  read_only
        .address_space:  global
        .offset:         64
        .size:           8
        .value_kind:     global_buffer
      - .actual_access:  read_only
        .address_space:  global
        .offset:         72
        .size:           8
        .value_kind:     global_buffer
      - .actual_access:  write_only
        .address_space:  global
        .offset:         80
        .size:           8
        .value_kind:     global_buffer
      - .actual_access:  write_only
        .address_space:  global
        .offset:         88
        .size:           8
        .value_kind:     global_buffer
    .group_segment_fixed_size: 161344
    .kernarg_segment_align: 8
    .kernarg_segment_size: 96
    .language:       OpenCL C
    .language_version:
      - 2
      - 0
    .max_flat_workgroup_size: 512
    .name:           _Z12pool1_kernelPKfS0_S0_S0_S0_S0_S0_S0_S0_S0_PfS1_
    .private_segment_fixed_size: 0
    .sgpr_count:     42
    .sgpr_spill_count: 0
    .symbol:         _Z12pool1_kernelPKfS0_S0_S0_S0_S0_S0_S0_S0_S0_PfS1_.kd
    .uniform_work_group_size: 1
    .uses_dynamic_stack: false
    .vgpr_count:     256
    .vgpr_spill_count: 0
    .wavefront_size: 64
  - .agpr_count:     0
    .args:
      - .actual_access:  read_only
        .address_space:  global
        .offset:         0
        .size:           8
        .value_kind:     global_buffer
      - .actual_access:  read_only
        .address_space:  global
        .offset:         8
        .size:           8
        .value_kind:     global_buffer
      - .address_space:  global
        .offset:         16
        .size:           8
        .value_kind:     global_buffer
    .group_segment_fixed_size: 18592
    .kernarg_segment_align: 8
    .kernarg_segment_size: 24
    .language:       OpenCL C
    .language_version:
      - 2
      - 0
    .max_flat_workgroup_size: 256
    .name:           _Z12pool3_kernelPKfS0_Pf
    .private_segment_fixed_size: 0
    .sgpr_count:     38
    .sgpr_spill_count: 0
    .symbol:         _Z12pool3_kernelPKfS0_Pf.kd
    .uniform_work_group_size: 1
    .uses_dynamic_stack: false
    .vgpr_count:     192
    .vgpr_spill_count: 0
    .wavefront_size: 64
